# RWKV scan waves: the 16 step pairs of a chunk fully unrolled with immediate LDS offsets, next pair's operands requested while the current pair computes, fma output chains, no loop-carried register cop
# speedup vs baseline: 1.0261x; 1.0066x over previous
; #define LAS __attribute__((address_space(3)))
; __device__ __forceinline__ void scan_unit(Frame& F, const Args& a, int layer, int unit) {
;     ...
;     if (wave < 4) {
;         f32x4 St[4]; v4u am[4], bm = (v4u){0u, 0u, 0u, 0u};
; #pragma unroll
;         for (int i = 0; i < 4; ++i) { St[i] = (f32x4){0.f, 0.f, 0.f, 0.f}; am[i] = (v4u){0u, 0u, 0u, 0u}; }
;         float sa0 = 0.f, sa1 = 0.f;
;         const unsigned m16 = lane < 16 ? 0xffffffffu : 0u;
;         LAS unsigned char* zblk = (LAS unsigned char*)(sY + 2 * SC_VEC);
;         if (tid < 8) ((LAS unsigned*)zblk)[tid] = 0u;
;         const int bkstep = lane < 16 ? 512 : 0;
;         for (int it = 0; it < NCH + 2; ++it) {
;             if (it >= 1 && it <= NCH) {
;                 const LAS float* bufc = bufs + ((it - 1) & 1) * SC_BUF;
;                 const LAS float* vqp = bufc + SC_VQ + 4 * (wave * 16 + (lane & 15));
;                 const LAS unsigned char* bkp = lane < 16 ? (const LAS unsigned char*)(bufc + SC_BK) + lane * 32 : (const LAS unsigned char*)zblk;
;                 LAS float* yb = lane < 16 ? sY + ((it - 1) & 1) * SC_VEC + wave * 16 + lane : (LAS float*)(zblk + 32);
;                 const int ystep = lane < 16 ? 64 : 0;
;                 if (it == 1) { sa0 = 0.f; sa1 = vqp[0] * bufc[SC_C + 16]; }
.LBB0_1336:
	s_and_b64 vcc, exec, s[0:1]
	s_cbranch_vccz .LBB0_1317
	v_cmp_gt_i32_e32 vcc, 8, v125
	s_and_saveexec_b64 s[0:1], vcc
	v_lshl_add_u32 v2, v125, 2, 0
	v_add_u32_e32 v2, 0x1b200, v2
	ds_write_b32 v2, v0
	s_or_b64 exec, exec, s[0:1]
	v_cmp_gt_i32_e64 s[40:41], 16, v1
	v_mov_b32_e32 v2, 0x200
	v_readlane_b32 s0, v253, 43
	v_cndmask_b32_e64 v144, 0, v2, s[40:41]
	v_or_b32_e32 v2, s74, v124
	v_lshlrev_b32_e32 v164, 5, v124
	v_lshlrev_b32_e32 v146, 5, v1
	v_lshl_add_u32 v147, v1, 2, s0
	v_and_b32_e32 v148, -16, v1
	v_lshlrev_b32_e32 v1, 7, v1
	v_lshlrev_b32_e32 v145, 4, v2
	v_cndmask_b32_e64 v2, 0, 64, s[40:41]
	v_and_b32_e32 v149, 0x180, v1
	v_readlane_b32 s0, v255, 4
	v_lshlrev_b32_e32 v153, 3, v2
	v_lshlrev_b32_e32 v154, 4, v2
	v_add3_u32 v150, v149, v148, s0
	v_readlane_b32 s0, v254, 40
	v_mul_u32_u24_e32 v155, 12, v2
	v_lshlrev_b32_e32 v156, 2, v2
	v_mov_b32_e32 v2, v0
	v_mov_b32_e32 v3, v0
	v_lshl_add_u32 v151, v124, 4, s0
	s_add_i32 s0, 0, 0x100
	v_mov_b32_e32 v1, v0
	v_mov_b64_e32 v[56:57], v[2:3]
	v_mov_b64_e32 v[60:61], v[2:3]
	v_mov_b64_e32 v[64:65], v[2:3]
	v_mov_b64_e32 v[68:69], v[2:3]
	s_mov_b32 s20, 0
	v_add_u32_e32 v152, s0, v148
	v_lshlrev_b32_e32 v157, 1, v144
	v_mov_b32_e32 v142, 0
	s_mov_b64 s[0:1], -1
	v_mov_b64_e32 v[54:55], v[0:1]
	v_mov_b64_e32 v[58:59], v[0:1]
	v_mov_b64_e32 v[62:63], v[0:1]
	v_mov_b64_e32 v[66:67], v[0:1]
	v_mov_b32_e32 v143, 0
	s_branch .LBB0_1341

; __device__ __forceinline__ void scan_load2(ScanOps& o, const LAS float* buf, const LAS float* vqp, const LAS unsigned char* bkp, int bkstep, int p, int lane) {
;     const int q = lane >> 4;
;     const LAS float* wp = buf + SC_WW + p * 64 + q * 4;
; #pragma unroll
;     for (int i = 0; i < 4; ++i) o.w[i] = *(const LAS f32x4*)(wp + 16 * i);
;     o.vq = *(const LAS f32x4*)(vqp + p * 256);
;     o.bk[0] = *(const LAS v4u*)(bkp + p * bkstep); o.bk[1] = *(const LAS v4u*)(bkp + p * bkstep + 16);
;     const LAS unsigned char* xp = (const LAS unsigned char*)(buf + SC_XA) + p * 512 + (lane & 3) * 128 + q * 16;
;     o.x[0] = *(const LAS bf16x8*)xp; o.x[1] = *(const LAS bf16x8*)(xp + 64);
; #pragma unroll
;     for (int i = 0; i < 4; ++i) o.c[i] = *(const LAS f32x4*)(buf + SC_C + p * 20 + 4 * i);
; }
; __device__ __forceinline__ const char* uni_ptr(const char* p) { const unsigned long long a = (unsigned long long)p;
;     const unsigned lo = (unsigned)__builtin_amdgcn_readfirstlane((int)(unsigned)a), hi = (unsigned)__builtin_amdgcn_readfirstlane((int)(unsigned)(a >> 32));
; __device__ __forceinline__ void scan_unit(Frame& F, const Args& a, int layer, int unit) {
;     ...
;         for (int it = 0; it < NCH + 2; ++it) {
;             if (it >= 1 && it <= NCH) {
;                 const LAS float* bufc = bufs + ((it - 1) & 1) * SC_BUF;
;                 const LAS float* vqp = bufc + SC_VQ + 4 * (wave * 16 + (lane & 15));
;                 const LAS unsigned char* bkp = lane < 16 ? (const LAS unsigned char*)(bufc + SC_BK) + lane * 32 : (const LAS unsigned char*)zblk;
;                 LAS float* yb = lane < 16 ? sY + ((it - 1) & 1) * SC_VEC + wave * 16 + lane : (LAS float*)(zblk + 32);
;                 const int ystep = lane < 16 ? 64 : 0;
;                 if (it == 1) { sa0 = 0.f; sa1 = vqp[0] * bufc[SC_C + 16]; }
;                 ScanOps o0, o1;
;                 scan_load2(o0, bufc, vqp, bkp, bkstep, 0, lane);
; #pragma unroll 1
;                 for (int p = 0; p < NPR; p += 2) {
;                     scan_load2(o1, bufc, vqp, bkp, bkstep, p + 1, lane);
;                     scan_pair(o0, St, sa0, sa1, am, bm, yb + (2 * p) * ystep, ystep, m16);
;                     if (p + 2 < NPR) scan_load2(o0, bufc, vqp, bkp, bkstep, p + 2, lane);
;                     scan_pair(o1, St, sa0, sa1, am, bm, yb + (2 * p + 2) * ystep, ystep, m16);
;                 }
.LBB0_1345:
	s_andn2_b64 vcc, exec, s[2:3]
	s_cbranch_vccnz .LBB0_1340
	s_andn2_b32 s3, 1, s20
	s_mul_i32 s2, s3, 0xb900
	s_cmp_lg_u32 s20, 1
	v_add_u32_e32 v159, s2, v145
	v_mov_b32_e32 v162, s2
	s_cbranch_scc1 .Lsc_go
	ds_read_b32 v2, v159 offset:4096
	ds_read_b32 v1, v162 offset:36928
	v_mov_b32_e32 v142, 0
	s_waitcnt lgkmcnt(0)
	v_mul_f32_e32 v143, v2, v1
.Lsc_go:
	v_add_u32_e32 v158, s2, v148
	v_add_u32_e32 v160, s2, v164
	v_add3_u32 v161, v149, v148, s2
	v_lshl_add_u32 v1, s3, 13, v147
	v_mov_b32_e32 v2, s95
	v_cndmask_b32_e64 v163, v2, v1, s[40:41]
	ds_read_b128 v[2:5], v158 offset:0
	ds_read_b128 v[6:9], v158 offset:64
	ds_read_b128 v[10:13], v158 offset:128
	ds_read_b128 v[14:17], v158 offset:192
	ds_read_b128 v[30:33], v161 offset:28672
	ds_read_b128 v[34:37], v161 offset:28736
	ds_read_b128 v[18:21], v159 offset:4096
	ds_read_b128 v[22:25], v160 offset:20480
	ds_read_b128 v[26:29], v160 offset:20496
	ds_read_b128 v[38:41], v162 offset:36864
	ds_read_b128 v[42:45], v162 offset:36880
	ds_read_b128 v[46:49], v162 offset:36896
	ds_read_b128 v[50:53], v162 offset:36912
	s_waitcnt lgkmcnt(0)
	ds_read_b128 v[70:73], v158 offset:256
	ds_read_b128 v[74:77], v158 offset:320
	ds_read_b128 v[78:81], v158 offset:384
	ds_read_b128 v[82:85], v158 offset:448
	ds_read_b128 v[98:101], v161 offset:29184
	ds_read_b128 v[102:105], v161 offset:29248
	ds_read_b128 v[86:89], v159 offset:5120
	ds_read_b128 v[90:93], v160 offset:20992
	ds_read_b128 v[94:97], v160 offset:21008
	ds_read_b128 v[106:109], v162 offset:36944
	ds_read_b128 v[110:113], v162 offset:36960
	ds_read_b128 v[114:117], v162 offset:36976
	ds_read_b128 v[118:121], v162 offset:36992
	v_cvt_pk_bf16_f32 v122, v54, v55
	v_cvt_pk_bf16_f32 v123, v56, v57
	v_cvt_pk_bf16_f32 v124, v58, v59
	v_cvt_pk_bf16_f32 v125, v60, v61
	v_cvt_pk_bf16_f32 v126, v62, v63
	v_cvt_pk_bf16_f32 v127, v64, v65
	v_cvt_pk_bf16_f32 v128, v66, v67
	v_cvt_pk_bf16_f32 v129, v68, v69
	v_mfma_f32_16x16x32_bf16 v[130:133], v[30:33], v[122:125], 0
	v_cvt_pk_bf16_f32 v136, v142, v18
	v_mfma_f32_16x16x32_bf16 v[130:133], v[34:37], v[126:129], v[130:133]
	v_cvt_pk_bf16_f32 v137, v143, v19
	v_cndmask_b32_e64 v134, 0, v136, s[40:41]
	v_cndmask_b32_e64 v135, 0, v137, s[40:41]
	v_mul_f32 v54, v54, v2
	v_mul_f32 v55, v55, v3
	v_mul_f32 v56, v56, v4
	v_mul_f32 v57, v57, v5
	v_mul_f32 v58, v58, v6
	v_mul_f32 v59, v59, v7
	v_mul_f32 v60, v60, v8
	v_mul_f32 v61, v61, v9
	v_mul_f32 v62, v62, v10
	v_mul_f32 v63, v63, v11
	v_mul_f32 v64, v64, v12
	v_mul_f32 v65, v65, v13
	v_mul_f32 v66, v66, v14
	v_mul_f32 v67, v67, v15
	v_mul_f32 v68, v68, v16
	v_mul_f32 v69, v69, v17
	v_mfma_f32_16x16x16_bf16 v[54:57], v[22:23], v[134:135], v[54:57]
	v_mfma_f32_16x16x16_bf16 v[58:61], v[24:25], v[134:135], v[58:61]
	v_mfma_f32_16x16x16_bf16 v[62:65], v[26:27], v[134:135], v[62:65]
	v_mfma_f32_16x16x16_bf16 v[66:69], v[28:29], v[134:135], v[66:69]
	v_fma_f32 v140, v142, v38, v130
	v_fma_f32 v141, v142, v42, v131
	v_fma_f32 v138, v142, v48, v132
	v_fma_f32 v139, v142, v50, v133
	v_fmac_f32_e32 v140, v39, v18
	v_fmac_f32_e32 v141, v43, v18
	v_fmac_f32_e32 v138, v49, v18
	v_fmac_f32_e32 v139, v51, v18
	v_fmac_f32_e32 v140, v143, v40
	v_fmac_f32_e32 v141, v143, v44
	ds_write_b32 v163, v138 offset:0
	v_fmac_f32_e32 v139, v143, v52
	v_fma_f32 v142, v41, v19, v140
	v_fmac_f32_e32 v141, v45, v19
	v_fmac_f32_e32 v139, v53, v19
	v_fmac_f32_e32 v141, v46, v142
	ds_write_b32 v163, v139 offset:256
	v_fma_f32 v143, v47, v20, v141
	s_waitcnt lgkmcnt(2)
	ds_read_b128 v[2:5], v158 offset:512
	ds_read_b128 v[6:9], v158 offset:576
	ds_read_b128 v[10:13], v158 offset:640
	ds_read_b128 v[14:17], v158 offset:704
	ds_read_b128 v[30:33], v161 offset:29696
	ds_read_b128 v[34:37], v161 offset:29760
	ds_read_b128 v[18:21], v159 offset:6144
	ds_read_b128 v[22:25], v160 offset:21504
	ds_read_b128 v[26:29], v160 offset:21520
	ds_read_b128 v[38:41], v162 offset:37024
	ds_read_b128 v[42:45], v162 offset:37040
	ds_read_b128 v[46:49], v162 offset:37056
	ds_read_b128 v[50:53], v162 offset:37072
	v_cvt_pk_bf16_f32 v122, v54, v55
	v_cvt_pk_bf16_f32 v123, v56, v57
	v_cvt_pk_bf16_f32 v124, v58, v59
	v_cvt_pk_bf16_f32 v125, v60, v61
	v_cvt_pk_bf16_f32 v126, v62, v63
	v_cvt_pk_bf16_f32 v127, v64, v65
	v_cvt_pk_bf16_f32 v128, v66, v67
	v_cvt_pk_bf16_f32 v129, v68, v69
	v_mfma_f32_16x16x32_bf16 v[130:133], v[98:101], v[122:125], 0
	v_cvt_pk_bf16_f32 v136, v142, v86
	v_mfma_f32_16x16x32_bf16 v[130:133], v[102:105], v[126:129], v[130:133]
	v_cvt_pk_bf16_f32 v137, v143, v87
	v_cndmask_b32_e64 v134, 0, v136, s[40:41]
	v_cndmask_b32_e64 v135, 0, v137, s[40:41]
	v_mul_f32 v54, v54, v70
	v_mul_f32 v55, v55, v71
	v_mul_f32 v56, v56, v72
	v_mul_f32 v57, v57, v73
	v_mul_f32 v58, v58, v74
	v_mul_f32 v59, v59, v75
	v_mul_f32 v60, v60, v76
	v_mul_f32 v61, v61, v77
	v_mul_f32 v62, v62, v78
	v_mul_f32 v63, v63, v79
	v_mul_f32 v64, v64, v80
	v_mul_f32 v65, v65, v81
	v_mul_f32 v66, v66, v82
	v_mul_f32 v67, v67, v83
	v_mul_f32 v68, v68, v84
	v_mul_f32 v69, v69, v85
	v_mfma_f32_16x16x16_bf16 v[54:57], v[90:91], v[134:135], v[54:57]
	v_mfma_f32_16x16x16_bf16 v[58:61], v[92:93], v[134:135], v[58:61]
	v_mfma_f32_16x16x16_bf16 v[62:65], v[94:95], v[134:135], v[62:65]
	v_mfma_f32_16x16x16_bf16 v[66:69], v[96:97], v[134:135], v[66:69]
	v_fma_f32 v140, v142, v106, v130
	v_fma_f32 v141, v142, v110, v131
	v_fma_f32 v138, v142, v116, v132
	v_fma_f32 v139, v142, v118, v133
	v_fmac_f32_e32 v140, v107, v86
	v_fmac_f32_e32 v141, v111, v86
	v_fmac_f32_e32 v138, v117, v86
	v_fmac_f32_e32 v139, v119, v86
	v_fmac_f32_e32 v140, v143, v108
	v_fmac_f32_e32 v141, v143, v112
	ds_write_b32 v163, v138 offset:512
	v_fmac_f32_e32 v139, v143, v120
	v_fma_f32 v142, v109, v87, v140
	v_fmac_f32_e32 v141, v113, v87
	v_fmac_f32_e32 v139, v121, v87
	v_fmac_f32_e32 v141, v114, v142
	ds_write_b32 v163, v139 offset:768
	v_fma_f32 v143, v115, v88, v141
	s_waitcnt lgkmcnt(2)
; __device__ __forceinline__ void scan_load2(ScanOps& o, const LAS float* buf, const LAS float* vqp, const LAS unsigned char* bkp, int bkstep, int p, int lane) {
;     const int q = lane >> 4;
;     const LAS float* wp = buf + SC_WW + p * 64 + q * 4;
; #pragma unroll
;     for (int i = 0; i < 4; ++i) o.w[i] = *(const LAS f32x4*)(wp + 16 * i);
;     o.vq = *(const LAS f32x4*)(vqp + p * 256);
;     o.bk[0] = *(const LAS v4u*)(bkp + p * bkstep); o.bk[1] = *(const LAS v4u*)(bkp + p * bkstep + 16);
;     const LAS unsigned char* xp = (const LAS unsigned char*)(buf + SC_XA) + p * 512 + (lane & 3) * 128 + q * 16;
;     o.x[0] = *(const LAS bf16x8*)xp; o.x[1] = *(const LAS bf16x8*)(xp + 64);
; #pragma unroll
;     for (int i = 0; i < 4; ++i) o.c[i] = *(const LAS f32x4*)(buf + SC_C + p * 20 + 4 * i);
; }
; __device__ __forceinline__ const char* uni_ptr(const char* p) { const unsigned long long a = (unsigned long long)p;
;     const unsigned lo = (unsigned)__builtin_amdgcn_readfirstlane((int)(unsigned)a), hi = (unsigned)__builtin_amdgcn_readfirstlane((int)(unsigned)(a >> 32));
;     return (const char*)(((unsigned long long)hi << 32) | lo); }
; __device__ __forceinline__ float smul(float a, float b) { float r; asm("v_mul_f32 %0, %1, %2" : "=v"(r) : "v"(a), "v"(b)); return r; }
; __device__ __forceinline__ void scan_pair(const ScanOps& o, f32x4 (&St)[4], float& sa0, float& sa1, v4u (&am)[4], v4u& bm, LAS float* ypt, int ystep, unsigned m16) {
;     v4u s0, s1;
;     s0.x = cvt_pk_bf16(St[0].x, St[0].y); s0.y = cvt_pk_bf16(St[0].z, St[0].w); s0.z = cvt_pk_bf16(St[1].x, St[1].y); s0.w = cvt_pk_bf16(St[1].z, St[1].w);
;     s1.x = cvt_pk_bf16(St[2].x, St[2].y); s1.y = cvt_pk_bf16(St[2].z, St[2].w); s1.z = cvt_pk_bf16(St[3].x, St[3].y); s1.w = cvt_pk_bf16(St[3].z, St[3].w);
;     f32x4 dv = (f32x4){0.f, 0.f, 0.f, 0.f};
;     dv = __builtin_amdgcn_mfma_f32_16x16x32_bf16(o.x[0], __builtin_bit_cast(bf16x8, s0), dv, 0, 0, 0);
;     dv = __builtin_amdgcn_mfma_f32_16x16x32_bf16(o.x[1], __builtin_bit_cast(bf16x8, s1), dv, 0, 0, 0);
;     const float v0 = o.vq.x, v1 = o.vq.y, v2 = o.vq.z;
;     typedef short s16x4 __attribute__((ext_vector_type(4)));
;     const v2u bm2 = (v2u){cvt_pk_bf16(sa0, v0) & m16, cvt_pk_bf16(sa1, v1) & m16};
; #pragma unroll
;     for (int i = 0; i < 4; ++i) { const v2u a2 = (v2u){o.bk[i >> 1][(i & 1) * 2], o.bk[i >> 1][(i & 1) * 2 + 1]};
	ds_read_b128 v[70:73], v158 offset:768
	ds_read_b128 v[74:77], v158 offset:832
	ds_read_b128 v[78:81], v158 offset:896
	ds_read_b128 v[82:85], v158 offset:960
	ds_read_b128 v[98:101], v161 offset:30208
	ds_read_b128 v[102:105], v161 offset:30272
	ds_read_b128 v[86:89], v159 offset:7168
	ds_read_b128 v[90:93], v160 offset:22016
	ds_read_b128 v[94:97], v160 offset:22032
	ds_read_b128 v[106:109], v162 offset:37104
	ds_read_b128 v[110:113], v162 offset:37120
	ds_read_b128 v[114:117], v162 offset:37136
	ds_read_b128 v[118:121], v162 offset:37152
	v_cvt_pk_bf16_f32 v122, v54, v55
	v_cvt_pk_bf16_f32 v123, v56, v57
	v_cvt_pk_bf16_f32 v124, v58, v59
	v_cvt_pk_bf16_f32 v125, v60, v61
	v_cvt_pk_bf16_f32 v126, v62, v63
	v_cvt_pk_bf16_f32 v127, v64, v65
	v_cvt_pk_bf16_f32 v128, v66, v67
	v_cvt_pk_bf16_f32 v129, v68, v69
	v_mfma_f32_16x16x32_bf16 v[130:133], v[30:33], v[122:125], 0
	v_cvt_pk_bf16_f32 v136, v142, v18
	v_mfma_f32_16x16x32_bf16 v[130:133], v[34:37], v[126:129], v[130:133]
	v_cvt_pk_bf16_f32 v137, v143, v19
	v_cndmask_b32_e64 v134, 0, v136, s[40:41]
	v_cndmask_b32_e64 v135, 0, v137, s[40:41]
	v_mul_f32 v54, v54, v2
	v_mul_f32 v55, v55, v3
	v_mul_f32 v56, v56, v4
	v_mul_f32 v57, v57, v5
	v_mul_f32 v58, v58, v6
	v_mul_f32 v59, v59, v7
	v_mul_f32 v60, v60, v8
	v_mul_f32 v61, v61, v9
	v_mul_f32 v62, v62, v10
	v_mul_f32 v63, v63, v11
	v_mul_f32 v64, v64, v12
	v_mul_f32 v65, v65, v13
	v_mul_f32 v66, v66, v14
	v_mul_f32 v67, v67, v15
	v_mul_f32 v68, v68, v16
	v_mul_f32 v69, v69, v17
	v_mfma_f32_16x16x16_bf16 v[54:57], v[22:23], v[134:135], v[54:57]
	v_mfma_f32_16x16x16_bf16 v[58:61], v[24:25], v[134:135], v[58:61]
	v_mfma_f32_16x16x16_bf16 v[62:65], v[26:27], v[134:135], v[62:65]
	v_mfma_f32_16x16x16_bf16 v[66:69], v[28:29], v[134:135], v[66:69]
	v_fma_f32 v140, v142, v38, v130
	v_fma_f32 v141, v142, v42, v131
	v_fma_f32 v138, v142, v48, v132
	v_fma_f32 v139, v142, v50, v133
	v_fmac_f32_e32 v140, v39, v18
	v_fmac_f32_e32 v141, v43, v18
	v_fmac_f32_e32 v138, v49, v18
	v_fmac_f32_e32 v139, v51, v18
	v_fmac_f32_e32 v140, v143, v40
	v_fmac_f32_e32 v141, v143, v44
	ds_write_b32 v163, v138 offset:1024
	v_fmac_f32_e32 v139, v143, v52
	v_fma_f32 v142, v41, v19, v140
	v_fmac_f32_e32 v141, v45, v19
	v_fmac_f32_e32 v139, v53, v19
	v_fmac_f32_e32 v141, v46, v142
	ds_write_b32 v163, v139 offset:1280
	v_fma_f32 v143, v47, v20, v141
	s_waitcnt lgkmcnt(2)
	ds_read_b128 v[2:5], v158 offset:1024
	ds_read_b128 v[6:9], v158 offset:1088
	ds_read_b128 v[10:13], v158 offset:1152
	ds_read_b128 v[14:17], v158 offset:1216
	ds_read_b128 v[30:33], v161 offset:30720
	ds_read_b128 v[34:37], v161 offset:30784
	ds_read_b128 v[18:21], v159 offset:8192
	ds_read_b128 v[22:25], v160 offset:22528
	ds_read_b128 v[26:29], v160 offset:22544
	ds_read_b128 v[38:41], v162 offset:37184
	ds_read_b128 v[42:45], v162 offset:37200
	ds_read_b128 v[46:49], v162 offset:37216
	ds_read_b128 v[50:53], v162 offset:37232
	v_cvt_pk_bf16_f32 v122, v54, v55
	v_cvt_pk_bf16_f32 v123, v56, v57
	v_cvt_pk_bf16_f32 v124, v58, v59
	v_cvt_pk_bf16_f32 v125, v60, v61
	v_cvt_pk_bf16_f32 v126, v62, v63
	v_cvt_pk_bf16_f32 v127, v64, v65
	v_cvt_pk_bf16_f32 v128, v66, v67
	v_cvt_pk_bf16_f32 v129, v68, v69
	v_mfma_f32_16x16x32_bf16 v[130:133], v[98:101], v[122:125], 0
	v_cvt_pk_bf16_f32 v136, v142, v86
	v_mfma_f32_16x16x32_bf16 v[130:133], v[102:105], v[126:129], v[130:133]
	v_cvt_pk_bf16_f32 v137, v143, v87
	v_cndmask_b32_e64 v134, 0, v136, s[40:41]
	v_cndmask_b32_e64 v135, 0, v137, s[40:41]
	v_mul_f32 v54, v54, v70
	v_mul_f32 v55, v55, v71
	v_mul_f32 v56, v56, v72
	v_mul_f32 v57, v57, v73
	v_mul_f32 v58, v58, v74
	v_mul_f32 v59, v59, v75
	v_mul_f32 v60, v60, v76
	v_mul_f32 v61, v61, v77
	v_mul_f32 v62, v62, v78
	v_mul_f32 v63, v63, v79
	v_mul_f32 v64, v64, v80
	v_mul_f32 v65, v65, v81
	v_mul_f32 v66, v66, v82
	v_mul_f32 v67, v67, v83
	v_mul_f32 v68, v68, v84
	v_mul_f32 v69, v69, v85
	v_mfma_f32_16x16x16_bf16 v[54:57], v[90:91], v[134:135], v[54:57]
	v_mfma_f32_16x16x16_bf16 v[58:61], v[92:93], v[134:135], v[58:61]
	v_mfma_f32_16x16x16_bf16 v[62:65], v[94:95], v[134:135], v[62:65]
	v_mfma_f32_16x16x16_bf16 v[66:69], v[96:97], v[134:135], v[66:69]
	v_fma_f32 v140, v142, v106, v130
	v_fma_f32 v141, v142, v110, v131
	v_fma_f32 v138, v142, v116, v132
	v_fma_f32 v139, v142, v118, v133
	v_fmac_f32_e32 v140, v107, v86
	v_fmac_f32_e32 v141, v111, v86
	v_fmac_f32_e32 v138, v117, v86
	v_fmac_f32_e32 v139, v119, v86
	v_fmac_f32_e32 v140, v143, v108
	v_fmac_f32_e32 v141, v143, v112
	ds_write_b32 v163, v138 offset:1536
	v_fmac_f32_e32 v139, v143, v120
	v_fma_f32 v142, v109, v87, v140
	v_fmac_f32_e32 v141, v113, v87
	v_fmac_f32_e32 v139, v121, v87
	v_fmac_f32_e32 v141, v114, v142
	ds_write_b32 v163, v139 offset:1792
	v_fma_f32 v143, v115, v88, v141
	s_waitcnt lgkmcnt(2)
; __device__ __forceinline__ void scan_load2(ScanOps& o, const LAS float* buf, const LAS float* vqp, const LAS unsigned char* bkp, int bkstep, int p, int lane) {
;     const int q = lane >> 4;
;     const LAS float* wp = buf + SC_WW + p * 64 + q * 4;
; #pragma unroll
;     for (int i = 0; i < 4; ++i) o.w[i] = *(const LAS f32x4*)(wp + 16 * i);
;     o.vq = *(const LAS f32x4*)(vqp + p * 256);
;     o.bk[0] = *(const LAS v4u*)(bkp + p * bkstep); o.bk[1] = *(const LAS v4u*)(bkp + p * bkstep + 16);
;     const LAS unsigned char* xp = (const LAS unsigned char*)(buf + SC_XA) + p * 512 + (lane & 3) * 128 + q * 16;
;     o.x[0] = *(const LAS bf16x8*)xp; o.x[1] = *(const LAS bf16x8*)(xp + 64);
; #pragma unroll
;     for (int i = 0; i < 4; ++i) o.c[i] = *(const LAS f32x4*)(buf + SC_C + p * 20 + 4 * i);
; }
; __device__ __forceinline__ const char* uni_ptr(const char* p) { const unsigned long long a = (unsigned long long)p;
;     const unsigned lo = (unsigned)__builtin_amdgcn_readfirstlane((int)(unsigned)a), hi = (unsigned)__builtin_amdgcn_readfirstlane((int)(unsigned)(a >> 32));
;     return (const char*)(((unsigned long long)hi << 32) | lo); }
; __device__ __forceinline__ float smul(float a, float b) { float r; asm("v_mul_f32 %0, %1, %2" : "=v"(r) : "v"(a), "v"(b)); return r; }
; __device__ __forceinline__ void scan_pair(const ScanOps& o, f32x4 (&St)[4], float& sa0, float& sa1, v4u (&am)[4], v4u& bm, LAS float* ypt, int ystep, unsigned m16) {
;     v4u s0, s1;
;     s0.x = cvt_pk_bf16(St[0].x, St[0].y); s0.y = cvt_pk_bf16(St[0].z, St[0].w); s0.z = cvt_pk_bf16(St[1].x, St[1].y); s0.w = cvt_pk_bf16(St[1].z, St[1].w);
;     s1.x = cvt_pk_bf16(St[2].x, St[2].y); s1.y = cvt_pk_bf16(St[2].z, St[2].w); s1.z = cvt_pk_bf16(St[3].x, St[3].y); s1.w = cvt_pk_bf16(St[3].z, St[3].w);
;     f32x4 dv = (f32x4){0.f, 0.f, 0.f, 0.f};
;     dv = __builtin_amdgcn_mfma_f32_16x16x32_bf16(o.x[0], __builtin_bit_cast(bf16x8, s0), dv, 0, 0, 0);
;     dv = __builtin_amdgcn_mfma_f32_16x16x32_bf16(o.x[1], __builtin_bit_cast(bf16x8, s1), dv, 0, 0, 0);
;     const float v0 = o.vq.x, v1 = o.vq.y, v2 = o.vq.z;
;     typedef short s16x4 __attribute__((ext_vector_type(4)));
;     const v2u bm2 = (v2u){cvt_pk_bf16(sa0, v0) & m16, cvt_pk_bf16(sa1, v1) & m16};
; #pragma unroll
;     for (int i = 0; i < 4; ++i) { const v2u a2 = (v2u){o.bk[i >> 1][(i & 1) * 2], o.bk[i >> 1][(i & 1) * 2 + 1]};
	ds_read_b128 v[70:73], v158 offset:1280
	ds_read_b128 v[74:77], v158 offset:1344
	ds_read_b128 v[78:81], v158 offset:1408
	ds_read_b128 v[82:85], v158 offset:1472
	ds_read_b128 v[98:101], v161 offset:31232
	ds_read_b128 v[102:105], v161 offset:31296
	ds_read_b128 v[86:89], v159 offset:9216
	ds_read_b128 v[90:93], v160 offset:23040
	ds_read_b128 v[94:97], v160 offset:23056
	ds_read_b128 v[106:109], v162 offset:37264
	ds_read_b128 v[110:113], v162 offset:37280
	ds_read_b128 v[114:117], v162 offset:37296
	ds_read_b128 v[118:121], v162 offset:37312
	v_cvt_pk_bf16_f32 v122, v54, v55
	v_cvt_pk_bf16_f32 v123, v56, v57
	v_cvt_pk_bf16_f32 v124, v58, v59
	v_cvt_pk_bf16_f32 v125, v60, v61
	v_cvt_pk_bf16_f32 v126, v62, v63
	v_cvt_pk_bf16_f32 v127, v64, v65
	v_cvt_pk_bf16_f32 v128, v66, v67
	v_cvt_pk_bf16_f32 v129, v68, v69
	v_mfma_f32_16x16x32_bf16 v[130:133], v[30:33], v[122:125], 0
	v_cvt_pk_bf16_f32 v136, v142, v18
	v_mfma_f32_16x16x32_bf16 v[130:133], v[34:37], v[126:129], v[130:133]
	v_cvt_pk_bf16_f32 v137, v143, v19
	v_cndmask_b32_e64 v134, 0, v136, s[40:41]
	v_cndmask_b32_e64 v135, 0, v137, s[40:41]
	v_mul_f32 v54, v54, v2
	v_mul_f32 v55, v55, v3
	v_mul_f32 v56, v56, v4
	v_mul_f32 v57, v57, v5
	v_mul_f32 v58, v58, v6
	v_mul_f32 v59, v59, v7
	v_mul_f32 v60, v60, v8
	v_mul_f32 v61, v61, v9
	v_mul_f32 v62, v62, v10
	v_mul_f32 v63, v63, v11
	v_mul_f32 v64, v64, v12
	v_mul_f32 v65, v65, v13
	v_mul_f32 v66, v66, v14
	v_mul_f32 v67, v67, v15
	v_mul_f32 v68, v68, v16
	v_mul_f32 v69, v69, v17
	v_mfma_f32_16x16x16_bf16 v[54:57], v[22:23], v[134:135], v[54:57]
	v_mfma_f32_16x16x16_bf16 v[58:61], v[24:25], v[134:135], v[58:61]
	v_mfma_f32_16x16x16_bf16 v[62:65], v[26:27], v[134:135], v[62:65]
	v_mfma_f32_16x16x16_bf16 v[66:69], v[28:29], v[134:135], v[66:69]
	v_fma_f32 v140, v142, v38, v130
	v_fma_f32 v141, v142, v42, v131
	v_fma_f32 v138, v142, v48, v132
	v_fma_f32 v139, v142, v50, v133
	v_fmac_f32_e32 v140, v39, v18
	v_fmac_f32_e32 v141, v43, v18
	v_fmac_f32_e32 v138, v49, v18
	v_fmac_f32_e32 v139, v51, v18
	v_fmac_f32_e32 v140, v143, v40
	v_fmac_f32_e32 v141, v143, v44
	ds_write_b32 v163, v138 offset:2048
	v_fmac_f32_e32 v139, v143, v52
	v_fma_f32 v142, v41, v19, v140
	v_fmac_f32_e32 v141, v45, v19
	v_fmac_f32_e32 v139, v53, v19
	v_fmac_f32_e32 v141, v46, v142
	ds_write_b32 v163, v139 offset:2304
	v_fma_f32 v143, v47, v20, v141
	s_waitcnt lgkmcnt(2)
	ds_read_b128 v[2:5], v158 offset:1536
	ds_read_b128 v[6:9], v158 offset:1600
	ds_read_b128 v[10:13], v158 offset:1664
	ds_read_b128 v[14:17], v158 offset:1728
	ds_read_b128 v[30:33], v161 offset:31744
	ds_read_b128 v[34:37], v161 offset:31808
	ds_read_b128 v[18:21], v159 offset:10240
	ds_read_b128 v[22:25], v160 offset:23552
	ds_read_b128 v[26:29], v160 offset:23568
	ds_read_b128 v[38:41], v162 offset:37344
	ds_read_b128 v[42:45], v162 offset:37360
	ds_read_b128 v[46:49], v162 offset:37376
	ds_read_b128 v[50:53], v162 offset:37392
	v_cvt_pk_bf16_f32 v122, v54, v55
	v_cvt_pk_bf16_f32 v123, v56, v57
	v_cvt_pk_bf16_f32 v124, v58, v59
	v_cvt_pk_bf16_f32 v125, v60, v61
	v_cvt_pk_bf16_f32 v126, v62, v63
	v_cvt_pk_bf16_f32 v127, v64, v65
	v_cvt_pk_bf16_f32 v128, v66, v67
	v_cvt_pk_bf16_f32 v129, v68, v69
	v_mfma_f32_16x16x32_bf16 v[130:133], v[98:101], v[122:125], 0
	v_cvt_pk_bf16_f32 v136, v142, v86
	v_mfma_f32_16x16x32_bf16 v[130:133], v[102:105], v[126:129], v[130:133]
	v_cvt_pk_bf16_f32 v137, v143, v87
	v_cndmask_b32_e64 v134, 0, v136, s[40:41]
	v_cndmask_b32_e64 v135, 0, v137, s[40:41]
	v_mul_f32 v54, v54, v70
	v_mul_f32 v55, v55, v71
	v_mul_f32 v56, v56, v72
	v_mul_f32 v57, v57, v73
	v_mul_f32 v58, v58, v74
	v_mul_f32 v59, v59, v75
	v_mul_f32 v60, v60, v76
	v_mul_f32 v61, v61, v77
	v_mul_f32 v62, v62, v78
	v_mul_f32 v63, v63, v79
	v_mul_f32 v64, v64, v80
	v_mul_f32 v65, v65, v81
	v_mul_f32 v66, v66, v82
	v_mul_f32 v67, v67, v83
	v_mul_f32 v68, v68, v84
	v_mul_f32 v69, v69, v85
	v_mfma_f32_16x16x16_bf16 v[54:57], v[90:91], v[134:135], v[54:57]
	v_mfma_f32_16x16x16_bf16 v[58:61], v[92:93], v[134:135], v[58:61]
	v_mfma_f32_16x16x16_bf16 v[62:65], v[94:95], v[134:135], v[62:65]
	v_mfma_f32_16x16x16_bf16 v[66:69], v[96:97], v[134:135], v[66:69]
	v_fma_f32 v140, v142, v106, v130
	v_fma_f32 v141, v142, v110, v131
	v_fma_f32 v138, v142, v116, v132
	v_fma_f32 v139, v142, v118, v133
	v_fmac_f32_e32 v140, v107, v86
	v_fmac_f32_e32 v141, v111, v86
	v_fmac_f32_e32 v138, v117, v86
	v_fmac_f32_e32 v139, v119, v86
	v_fmac_f32_e32 v140, v143, v108
	v_fmac_f32_e32 v141, v143, v112
	ds_write_b32 v163, v138 offset:2560
	v_fmac_f32_e32 v139, v143, v120
	v_fma_f32 v142, v109, v87, v140
	v_fmac_f32_e32 v141, v113, v87
	v_fmac_f32_e32 v139, v121, v87
	v_fmac_f32_e32 v141, v114, v142
	ds_write_b32 v163, v139 offset:2816
	v_fma_f32 v143, v115, v88, v141
	s_waitcnt lgkmcnt(2)
; __device__ __forceinline__ void scan_load2(ScanOps& o, const LAS float* buf, const LAS float* vqp, const LAS unsigned char* bkp, int bkstep, int p, int lane) {
;     const int q = lane >> 4;
;     const LAS float* wp = buf + SC_WW + p * 64 + q * 4;
; #pragma unroll
;     for (int i = 0; i < 4; ++i) o.w[i] = *(const LAS f32x4*)(wp + 16 * i);
;     o.vq = *(const LAS f32x4*)(vqp + p * 256);
;     o.bk[0] = *(const LAS v4u*)(bkp + p * bkstep); o.bk[1] = *(const LAS v4u*)(bkp + p * bkstep + 16);
;     const LAS unsigned char* xp = (const LAS unsigned char*)(buf + SC_XA) + p * 512 + (lane & 3) * 128 + q * 16;
;     o.x[0] = *(const LAS bf16x8*)xp; o.x[1] = *(const LAS bf16x8*)(xp + 64);
; #pragma unroll
;     for (int i = 0; i < 4; ++i) o.c[i] = *(const LAS f32x4*)(buf + SC_C + p * 20 + 4 * i);
; }
; __device__ __forceinline__ const char* uni_ptr(const char* p) { const unsigned long long a = (unsigned long long)p;
;     const unsigned lo = (unsigned)__builtin_amdgcn_readfirstlane((int)(unsigned)a), hi = (unsigned)__builtin_amdgcn_readfirstlane((int)(unsigned)(a >> 32));
;     return (const char*)(((unsigned long long)hi << 32) | lo); }
; __device__ __forceinline__ float smul(float a, float b) { float r; asm("v_mul_f32 %0, %1, %2" : "=v"(r) : "v"(a), "v"(b)); return r; }
; __device__ __forceinline__ void scan_pair(const ScanOps& o, f32x4 (&St)[4], float& sa0, float& sa1, v4u (&am)[4], v4u& bm, LAS float* ypt, int ystep, unsigned m16) {
;     v4u s0, s1;
;     s0.x = cvt_pk_bf16(St[0].x, St[0].y); s0.y = cvt_pk_bf16(St[0].z, St[0].w); s0.z = cvt_pk_bf16(St[1].x, St[1].y); s0.w = cvt_pk_bf16(St[1].z, St[1].w);
;     s1.x = cvt_pk_bf16(St[2].x, St[2].y); s1.y = cvt_pk_bf16(St[2].z, St[2].w); s1.z = cvt_pk_bf16(St[3].x, St[3].y); s1.w = cvt_pk_bf16(St[3].z, St[3].w);
;     f32x4 dv = (f32x4){0.f, 0.f, 0.f, 0.f};
;     dv = __builtin_amdgcn_mfma_f32_16x16x32_bf16(o.x[0], __builtin_bit_cast(bf16x8, s0), dv, 0, 0, 0);
;     dv = __builtin_amdgcn_mfma_f32_16x16x32_bf16(o.x[1], __builtin_bit_cast(bf16x8, s1), dv, 0, 0, 0);
;     const float v0 = o.vq.x, v1 = o.vq.y, v2 = o.vq.z;
;     typedef short s16x4 __attribute__((ext_vector_type(4)));
;     const v2u bm2 = (v2u){cvt_pk_bf16(sa0, v0) & m16, cvt_pk_bf16(sa1, v1) & m16};
; #pragma unroll
;     for (int i = 0; i < 4; ++i) { const v2u a2 = (v2u){o.bk[i >> 1][(i & 1) * 2], o.bk[i >> 1][(i & 1) * 2 + 1]};
	ds_read_b128 v[70:73], v158 offset:1792
	ds_read_b128 v[74:77], v158 offset:1856
	ds_read_b128 v[78:81], v158 offset:1920
	ds_read_b128 v[82:85], v158 offset:1984
	ds_read_b128 v[98:101], v161 offset:32256
	ds_read_b128 v[102:105], v161 offset:32320
	ds_read_b128 v[86:89], v159 offset:11264
	ds_read_b128 v[90:93], v160 offset:24064
	ds_read_b128 v[94:97], v160 offset:24080
	ds_read_b128 v[106:109], v162 offset:37424
	ds_read_b128 v[110:113], v162 offset:37440
	ds_read_b128 v[114:117], v162 offset:37456
	ds_read_b128 v[118:121], v162 offset:37472
	v_cvt_pk_bf16_f32 v122, v54, v55
	v_cvt_pk_bf16_f32 v123, v56, v57
	v_cvt_pk_bf16_f32 v124, v58, v59
	v_cvt_pk_bf16_f32 v125, v60, v61
	v_cvt_pk_bf16_f32 v126, v62, v63
	v_cvt_pk_bf16_f32 v127, v64, v65
	v_cvt_pk_bf16_f32 v128, v66, v67
	v_cvt_pk_bf16_f32 v129, v68, v69
	v_mfma_f32_16x16x32_bf16 v[130:133], v[30:33], v[122:125], 0
	v_cvt_pk_bf16_f32 v136, v142, v18
	v_mfma_f32_16x16x32_bf16 v[130:133], v[34:37], v[126:129], v[130:133]
	v_cvt_pk_bf16_f32 v137, v143, v19
	v_cndmask_b32_e64 v134, 0, v136, s[40:41]
	v_cndmask_b32_e64 v135, 0, v137, s[40:41]
	v_mul_f32 v54, v54, v2
	v_mul_f32 v55, v55, v3
	v_mul_f32 v56, v56, v4
	v_mul_f32 v57, v57, v5
	v_mul_f32 v58, v58, v6
	v_mul_f32 v59, v59, v7
	v_mul_f32 v60, v60, v8
	v_mul_f32 v61, v61, v9
	v_mul_f32 v62, v62, v10
	v_mul_f32 v63, v63, v11
	v_mul_f32 v64, v64, v12
	v_mul_f32 v65, v65, v13
	v_mul_f32 v66, v66, v14
	v_mul_f32 v67, v67, v15
	v_mul_f32 v68, v68, v16
	v_mul_f32 v69, v69, v17
	v_mfma_f32_16x16x16_bf16 v[54:57], v[22:23], v[134:135], v[54:57]
	v_mfma_f32_16x16x16_bf16 v[58:61], v[24:25], v[134:135], v[58:61]
	v_mfma_f32_16x16x16_bf16 v[62:65], v[26:27], v[134:135], v[62:65]
	v_mfma_f32_16x16x16_bf16 v[66:69], v[28:29], v[134:135], v[66:69]
	v_fma_f32 v140, v142, v38, v130
	v_fma_f32 v141, v142, v42, v131
	v_fma_f32 v138, v142, v48, v132
	v_fma_f32 v139, v142, v50, v133
	v_fmac_f32_e32 v140, v39, v18
	v_fmac_f32_e32 v141, v43, v18
	v_fmac_f32_e32 v138, v49, v18
	v_fmac_f32_e32 v139, v51, v18
	v_fmac_f32_e32 v140, v143, v40
	v_fmac_f32_e32 v141, v143, v44
	ds_write_b32 v163, v138 offset:3072
	v_fmac_f32_e32 v139, v143, v52
	v_fma_f32 v142, v41, v19, v140
	v_fmac_f32_e32 v141, v45, v19
	v_fmac_f32_e32 v139, v53, v19
	v_fmac_f32_e32 v141, v46, v142
	ds_write_b32 v163, v139 offset:3328
	v_fma_f32 v143, v47, v20, v141
	s_waitcnt lgkmcnt(2)
	ds_read_b128 v[2:5], v158 offset:2048
	ds_read_b128 v[6:9], v158 offset:2112
	ds_read_b128 v[10:13], v158 offset:2176
	ds_read_b128 v[14:17], v158 offset:2240
	ds_read_b128 v[30:33], v161 offset:32768
	ds_read_b128 v[34:37], v161 offset:32832
	ds_read_b128 v[18:21], v159 offset:12288
	ds_read_b128 v[22:25], v160 offset:24576
	ds_read_b128 v[26:29], v160 offset:24592
	ds_read_b128 v[38:41], v162 offset:37504
	ds_read_b128 v[42:45], v162 offset:37520
	ds_read_b128 v[46:49], v162 offset:37536
	ds_read_b128 v[50:53], v162 offset:37552
	v_cvt_pk_bf16_f32 v122, v54, v55
	v_cvt_pk_bf16_f32 v123, v56, v57
	v_cvt_pk_bf16_f32 v124, v58, v59
	v_cvt_pk_bf16_f32 v125, v60, v61
	v_cvt_pk_bf16_f32 v126, v62, v63
	v_cvt_pk_bf16_f32 v127, v64, v65
	v_cvt_pk_bf16_f32 v128, v66, v67
	v_cvt_pk_bf16_f32 v129, v68, v69
	v_mfma_f32_16x16x32_bf16 v[130:133], v[98:101], v[122:125], 0
	v_cvt_pk_bf16_f32 v136, v142, v86
	v_mfma_f32_16x16x32_bf16 v[130:133], v[102:105], v[126:129], v[130:133]
	v_cvt_pk_bf16_f32 v137, v143, v87
	v_cndmask_b32_e64 v134, 0, v136, s[40:41]
	v_cndmask_b32_e64 v135, 0, v137, s[40:41]
	v_mul_f32 v54, v54, v70
	v_mul_f32 v55, v55, v71
	v_mul_f32 v56, v56, v72
	v_mul_f32 v57, v57, v73
	v_mul_f32 v58, v58, v74
	v_mul_f32 v59, v59, v75
	v_mul_f32 v60, v60, v76
	v_mul_f32 v61, v61, v77
	v_mul_f32 v62, v62, v78
	v_mul_f32 v63, v63, v79
	v_mul_f32 v64, v64, v80
	v_mul_f32 v65, v65, v81
	v_mul_f32 v66, v66, v82
	v_mul_f32 v67, v67, v83
	v_mul_f32 v68, v68, v84
	v_mul_f32 v69, v69, v85
	v_mfma_f32_16x16x16_bf16 v[54:57], v[90:91], v[134:135], v[54:57]
	v_mfma_f32_16x16x16_bf16 v[58:61], v[92:93], v[134:135], v[58:61]
	v_mfma_f32_16x16x16_bf16 v[62:65], v[94:95], v[134:135], v[62:65]
	v_mfma_f32_16x16x16_bf16 v[66:69], v[96:97], v[134:135], v[66:69]
	v_fma_f32 v140, v142, v106, v130
	v_fma_f32 v141, v142, v110, v131
	v_fma_f32 v138, v142, v116, v132
	v_fma_f32 v139, v142, v118, v133
	v_fmac_f32_e32 v140, v107, v86
	v_fmac_f32_e32 v141, v111, v86
	v_fmac_f32_e32 v138, v117, v86
	v_fmac_f32_e32 v139, v119, v86
	v_fmac_f32_e32 v140, v143, v108
	v_fmac_f32_e32 v141, v143, v112
	ds_write_b32 v163, v138 offset:3584
	v_fmac_f32_e32 v139, v143, v120
	v_fma_f32 v142, v109, v87, v140
	v_fmac_f32_e32 v141, v113, v87
	v_fmac_f32_e32 v139, v121, v87
	v_fmac_f32_e32 v141, v114, v142
	ds_write_b32 v163, v139 offset:3840
	v_fma_f32 v143, v115, v88, v141
	s_waitcnt lgkmcnt(2)
; __device__ __forceinline__ void scan_load2(ScanOps& o, const LAS float* buf, const LAS float* vqp, const LAS unsigned char* bkp, int bkstep, int p, int lane) {
;     const int q = lane >> 4;
;     const LAS float* wp = buf + SC_WW + p * 64 + q * 4;
; #pragma unroll
;     for (int i = 0; i < 4; ++i) o.w[i] = *(const LAS f32x4*)(wp + 16 * i);
;     o.vq = *(const LAS f32x4*)(vqp + p * 256);
;     o.bk[0] = *(const LAS v4u*)(bkp + p * bkstep); o.bk[1] = *(const LAS v4u*)(bkp + p * bkstep + 16);
;     const LAS unsigned char* xp = (const LAS unsigned char*)(buf + SC_XA) + p * 512 + (lane & 3) * 128 + q * 16;
;     o.x[0] = *(const LAS bf16x8*)xp; o.x[1] = *(const LAS bf16x8*)(xp + 64);
; #pragma unroll
;     for (int i = 0; i < 4; ++i) o.c[i] = *(const LAS f32x4*)(buf + SC_C + p * 20 + 4 * i);
; }
; __device__ __forceinline__ const char* uni_ptr(const char* p) { const unsigned long long a = (unsigned long long)p;
;     const unsigned lo = (unsigned)__builtin_amdgcn_readfirstlane((int)(unsigned)a), hi = (unsigned)__builtin_amdgcn_readfirstlane((int)(unsigned)(a >> 32));
;     return (const char*)(((unsigned long long)hi << 32) | lo); }
; __device__ __forceinline__ float smul(float a, float b) { float r; asm("v_mul_f32 %0, %1, %2" : "=v"(r) : "v"(a), "v"(b)); return r; }
; __device__ __forceinline__ void scan_pair(const ScanOps& o, f32x4 (&St)[4], float& sa0, float& sa1, v4u (&am)[4], v4u& bm, LAS float* ypt, int ystep, unsigned m16) {
;     v4u s0, s1;
;     s0.x = cvt_pk_bf16(St[0].x, St[0].y); s0.y = cvt_pk_bf16(St[0].z, St[0].w); s0.z = cvt_pk_bf16(St[1].x, St[1].y); s0.w = cvt_pk_bf16(St[1].z, St[1].w);
;     s1.x = cvt_pk_bf16(St[2].x, St[2].y); s1.y = cvt_pk_bf16(St[2].z, St[2].w); s1.z = cvt_pk_bf16(St[3].x, St[3].y); s1.w = cvt_pk_bf16(St[3].z, St[3].w);
;     f32x4 dv = (f32x4){0.f, 0.f, 0.f, 0.f};
;     dv = __builtin_amdgcn_mfma_f32_16x16x32_bf16(o.x[0], __builtin_bit_cast(bf16x8, s0), dv, 0, 0, 0);
;     dv = __builtin_amdgcn_mfma_f32_16x16x32_bf16(o.x[1], __builtin_bit_cast(bf16x8, s1), dv, 0, 0, 0);
;     const float v0 = o.vq.x, v1 = o.vq.y, v2 = o.vq.z;
;     typedef short s16x4 __attribute__((ext_vector_type(4)));
;     const v2u bm2 = (v2u){cvt_pk_bf16(sa0, v0) & m16, cvt_pk_bf16(sa1, v1) & m16};
; #pragma unroll
;     for (int i = 0; i < 4; ++i) { const v2u a2 = (v2u){o.bk[i >> 1][(i & 1) * 2], o.bk[i >> 1][(i & 1) * 2 + 1]};
	ds_read_b128 v[70:73], v158 offset:2304
	ds_read_b128 v[74:77], v158 offset:2368
	ds_read_b128 v[78:81], v158 offset:2432
	ds_read_b128 v[82:85], v158 offset:2496
	ds_read_b128 v[98:101], v161 offset:33280
	ds_read_b128 v[102:105], v161 offset:33344
	ds_read_b128 v[86:89], v159 offset:13312
	ds_read_b128 v[90:93], v160 offset:25088
	ds_read_b128 v[94:97], v160 offset:25104
	ds_read_b128 v[106:109], v162 offset:37584
	ds_read_b128 v[110:113], v162 offset:37600
	ds_read_b128 v[114:117], v162 offset:37616
	ds_read_b128 v[118:121], v162 offset:37632
	v_cvt_pk_bf16_f32 v122, v54, v55
	v_cvt_pk_bf16_f32 v123, v56, v57
	v_cvt_pk_bf16_f32 v124, v58, v59
	v_cvt_pk_bf16_f32 v125, v60, v61
	v_cvt_pk_bf16_f32 v126, v62, v63
	v_cvt_pk_bf16_f32 v127, v64, v65
	v_cvt_pk_bf16_f32 v128, v66, v67
	v_cvt_pk_bf16_f32 v129, v68, v69
	v_mfma_f32_16x16x32_bf16 v[130:133], v[30:33], v[122:125], 0
	v_cvt_pk_bf16_f32 v136, v142, v18
	v_mfma_f32_16x16x32_bf16 v[130:133], v[34:37], v[126:129], v[130:133]
	v_cvt_pk_bf16_f32 v137, v143, v19
	v_cndmask_b32_e64 v134, 0, v136, s[40:41]
	v_cndmask_b32_e64 v135, 0, v137, s[40:41]
	v_mul_f32 v54, v54, v2
	v_mul_f32 v55, v55, v3
	v_mul_f32 v56, v56, v4
	v_mul_f32 v57, v57, v5
	v_mul_f32 v58, v58, v6
	v_mul_f32 v59, v59, v7
	v_mul_f32 v60, v60, v8
	v_mul_f32 v61, v61, v9
	v_mul_f32 v62, v62, v10
	v_mul_f32 v63, v63, v11
	v_mul_f32 v64, v64, v12
	v_mul_f32 v65, v65, v13
	v_mul_f32 v66, v66, v14
	v_mul_f32 v67, v67, v15
	v_mul_f32 v68, v68, v16
	v_mul_f32 v69, v69, v17
	v_mfma_f32_16x16x16_bf16 v[54:57], v[22:23], v[134:135], v[54:57]
	v_mfma_f32_16x16x16_bf16 v[58:61], v[24:25], v[134:135], v[58:61]
	v_mfma_f32_16x16x16_bf16 v[62:65], v[26:27], v[134:135], v[62:65]
	v_mfma_f32_16x16x16_bf16 v[66:69], v[28:29], v[134:135], v[66:69]
	v_fma_f32 v140, v142, v38, v130
	v_fma_f32 v141, v142, v42, v131
	v_fma_f32 v138, v142, v48, v132
	v_fma_f32 v139, v142, v50, v133
	v_fmac_f32_e32 v140, v39, v18
	v_fmac_f32_e32 v141, v43, v18
	v_fmac_f32_e32 v138, v49, v18
	v_fmac_f32_e32 v139, v51, v18
	v_fmac_f32_e32 v140, v143, v40
	v_fmac_f32_e32 v141, v143, v44
	ds_write_b32 v163, v138 offset:4096
	v_fmac_f32_e32 v139, v143, v52
	v_fma_f32 v142, v41, v19, v140
	v_fmac_f32_e32 v141, v45, v19
	v_fmac_f32_e32 v139, v53, v19
	v_fmac_f32_e32 v141, v46, v142
	ds_write_b32 v163, v139 offset:4352
	v_fma_f32 v143, v47, v20, v141
	s_waitcnt lgkmcnt(2)
	ds_read_b128 v[2:5], v158 offset:2560
	ds_read_b128 v[6:9], v158 offset:2624
	ds_read_b128 v[10:13], v158 offset:2688
	ds_read_b128 v[14:17], v158 offset:2752
	ds_read_b128 v[30:33], v161 offset:33792
	ds_read_b128 v[34:37], v161 offset:33856
	ds_read_b128 v[18:21], v159 offset:14336
	ds_read_b128 v[22:25], v160 offset:25600
	ds_read_b128 v[26:29], v160 offset:25616
	ds_read_b128 v[38:41], v162 offset:37664
	ds_read_b128 v[42:45], v162 offset:37680
	ds_read_b128 v[46:49], v162 offset:37696
	ds_read_b128 v[50:53], v162 offset:37712
	v_cvt_pk_bf16_f32 v122, v54, v55
	v_cvt_pk_bf16_f32 v123, v56, v57
	v_cvt_pk_bf16_f32 v124, v58, v59
	v_cvt_pk_bf16_f32 v125, v60, v61
	v_cvt_pk_bf16_f32 v126, v62, v63
	v_cvt_pk_bf16_f32 v127, v64, v65
	v_cvt_pk_bf16_f32 v128, v66, v67
	v_cvt_pk_bf16_f32 v129, v68, v69
	v_mfma_f32_16x16x32_bf16 v[130:133], v[98:101], v[122:125], 0
	v_cvt_pk_bf16_f32 v136, v142, v86
	v_mfma_f32_16x16x32_bf16 v[130:133], v[102:105], v[126:129], v[130:133]
	v_cvt_pk_bf16_f32 v137, v143, v87
	v_cndmask_b32_e64 v134, 0, v136, s[40:41]
	v_cndmask_b32_e64 v135, 0, v137, s[40:41]
	v_mul_f32 v54, v54, v70
	v_mul_f32 v55, v55, v71
	v_mul_f32 v56, v56, v72
	v_mul_f32 v57, v57, v73
	v_mul_f32 v58, v58, v74
	v_mul_f32 v59, v59, v75
	v_mul_f32 v60, v60, v76
	v_mul_f32 v61, v61, v77
	v_mul_f32 v62, v62, v78
	v_mul_f32 v63, v63, v79
	v_mul_f32 v64, v64, v80
	v_mul_f32 v65, v65, v81
	v_mul_f32 v66, v66, v82
	v_mul_f32 v67, v67, v83
	v_mul_f32 v68, v68, v84
	v_mul_f32 v69, v69, v85
	v_mfma_f32_16x16x16_bf16 v[54:57], v[90:91], v[134:135], v[54:57]
	v_mfma_f32_16x16x16_bf16 v[58:61], v[92:93], v[134:135], v[58:61]
	v_mfma_f32_16x16x16_bf16 v[62:65], v[94:95], v[134:135], v[62:65]
	v_mfma_f32_16x16x16_bf16 v[66:69], v[96:97], v[134:135], v[66:69]
	v_fma_f32 v140, v142, v106, v130
	v_fma_f32 v141, v142, v110, v131
	v_fma_f32 v138, v142, v116, v132
	v_fma_f32 v139, v142, v118, v133
	v_fmac_f32_e32 v140, v107, v86
	v_fmac_f32_e32 v141, v111, v86
	v_fmac_f32_e32 v138, v117, v86
	v_fmac_f32_e32 v139, v119, v86
	v_fmac_f32_e32 v140, v143, v108
	v_fmac_f32_e32 v141, v143, v112
	ds_write_b32 v163, v138 offset:4608
	v_fmac_f32_e32 v139, v143, v120
	v_fma_f32 v142, v109, v87, v140
	v_fmac_f32_e32 v141, v113, v87
	v_fmac_f32_e32 v139, v121, v87
	v_fmac_f32_e32 v141, v114, v142
	ds_write_b32 v163, v139 offset:4864
	v_fma_f32 v143, v115, v88, v141
	s_waitcnt lgkmcnt(2)
; __device__ __forceinline__ void scan_load2(ScanOps& o, const LAS float* buf, const LAS float* vqp, const LAS unsigned char* bkp, int bkstep, int p, int lane) {
;     const int q = lane >> 4;
;     const LAS float* wp = buf + SC_WW + p * 64 + q * 4;
; #pragma unroll
;     for (int i = 0; i < 4; ++i) o.w[i] = *(const LAS f32x4*)(wp + 16 * i);
;     o.vq = *(const LAS f32x4*)(vqp + p * 256);
;     o.bk[0] = *(const LAS v4u*)(bkp + p * bkstep); o.bk[1] = *(const LAS v4u*)(bkp + p * bkstep + 16);
;     const LAS unsigned char* xp = (const LAS unsigned char*)(buf + SC_XA) + p * 512 + (lane & 3) * 128 + q * 16;
;     o.x[0] = *(const LAS bf16x8*)xp; o.x[1] = *(const LAS bf16x8*)(xp + 64);
; #pragma unroll
;     for (int i = 0; i < 4; ++i) o.c[i] = *(const LAS f32x4*)(buf + SC_C + p * 20 + 4 * i);
; }
; __device__ __forceinline__ const char* uni_ptr(const char* p) { const unsigned long long a = (unsigned long long)p;
;     const unsigned lo = (unsigned)__builtin_amdgcn_readfirstlane((int)(unsigned)a), hi = (unsigned)__builtin_amdgcn_readfirstlane((int)(unsigned)(a >> 32));
;     return (const char*)(((unsigned long long)hi << 32) | lo); }
; __device__ __forceinline__ float smul(float a, float b) { float r; asm("v_mul_f32 %0, %1, %2" : "=v"(r) : "v"(a), "v"(b)); return r; }
; __device__ __forceinline__ void scan_pair(const ScanOps& o, f32x4 (&St)[4], float& sa0, float& sa1, v4u (&am)[4], v4u& bm, LAS float* ypt, int ystep, unsigned m16) {
;     v4u s0, s1;
;     s0.x = cvt_pk_bf16(St[0].x, St[0].y); s0.y = cvt_pk_bf16(St[0].z, St[0].w); s0.z = cvt_pk_bf16(St[1].x, St[1].y); s0.w = cvt_pk_bf16(St[1].z, St[1].w);
;     s1.x = cvt_pk_bf16(St[2].x, St[2].y); s1.y = cvt_pk_bf16(St[2].z, St[2].w); s1.z = cvt_pk_bf16(St[3].x, St[3].y); s1.w = cvt_pk_bf16(St[3].z, St[3].w);
;     f32x4 dv = (f32x4){0.f, 0.f, 0.f, 0.f};
;     dv = __builtin_amdgcn_mfma_f32_16x16x32_bf16(o.x[0], __builtin_bit_cast(bf16x8, s0), dv, 0, 0, 0);
;     dv = __builtin_amdgcn_mfma_f32_16x16x32_bf16(o.x[1], __builtin_bit_cast(bf16x8, s1), dv, 0, 0, 0);
;     const float v0 = o.vq.x, v1 = o.vq.y, v2 = o.vq.z;
;     typedef short s16x4 __attribute__((ext_vector_type(4)));
;     const v2u bm2 = (v2u){cvt_pk_bf16(sa0, v0) & m16, cvt_pk_bf16(sa1, v1) & m16};
; #pragma unroll
;     for (int i = 0; i < 4; ++i) { const v2u a2 = (v2u){o.bk[i >> 1][(i & 1) * 2], o.bk[i >> 1][(i & 1) * 2 + 1]};
	ds_read_b128 v[70:73], v158 offset:2816
	ds_read_b128 v[74:77], v158 offset:2880
	ds_read_b128 v[78:81], v158 offset:2944
	ds_read_b128 v[82:85], v158 offset:3008
	ds_read_b128 v[98:101], v161 offset:34304
	ds_read_b128 v[102:105], v161 offset:34368
	ds_read_b128 v[86:89], v159 offset:15360
	ds_read_b128 v[90:93], v160 offset:26112
	ds_read_b128 v[94:97], v160 offset:26128
	ds_read_b128 v[106:109], v162 offset:37744
	ds_read_b128 v[110:113], v162 offset:37760
	ds_read_b128 v[114:117], v162 offset:37776
	ds_read_b128 v[118:121], v162 offset:37792
	v_cvt_pk_bf16_f32 v122, v54, v55
	v_cvt_pk_bf16_f32 v123, v56, v57
	v_cvt_pk_bf16_f32 v124, v58, v59
	v_cvt_pk_bf16_f32 v125, v60, v61
	v_cvt_pk_bf16_f32 v126, v62, v63
	v_cvt_pk_bf16_f32 v127, v64, v65
	v_cvt_pk_bf16_f32 v128, v66, v67
	v_cvt_pk_bf16_f32 v129, v68, v69
	v_mfma_f32_16x16x32_bf16 v[130:133], v[30:33], v[122:125], 0
	v_cvt_pk_bf16_f32 v136, v142, v18
	v_mfma_f32_16x16x32_bf16 v[130:133], v[34:37], v[126:129], v[130:133]
	v_cvt_pk_bf16_f32 v137, v143, v19
	v_cndmask_b32_e64 v134, 0, v136, s[40:41]
	v_cndmask_b32_e64 v135, 0, v137, s[40:41]
	v_mul_f32 v54, v54, v2
	v_mul_f32 v55, v55, v3
	v_mul_f32 v56, v56, v4
	v_mul_f32 v57, v57, v5
	v_mul_f32 v58, v58, v6
	v_mul_f32 v59, v59, v7
	v_mul_f32 v60, v60, v8
	v_mul_f32 v61, v61, v9
	v_mul_f32 v62, v62, v10
	v_mul_f32 v63, v63, v11
	v_mul_f32 v64, v64, v12
	v_mul_f32 v65, v65, v13
	v_mul_f32 v66, v66, v14
	v_mul_f32 v67, v67, v15
	v_mul_f32 v68, v68, v16
	v_mul_f32 v69, v69, v17
	v_mfma_f32_16x16x16_bf16 v[54:57], v[22:23], v[134:135], v[54:57]
	v_mfma_f32_16x16x16_bf16 v[58:61], v[24:25], v[134:135], v[58:61]
	v_mfma_f32_16x16x16_bf16 v[62:65], v[26:27], v[134:135], v[62:65]
	v_mfma_f32_16x16x16_bf16 v[66:69], v[28:29], v[134:135], v[66:69]
	v_fma_f32 v140, v142, v38, v130
	v_fma_f32 v141, v142, v42, v131
	v_fma_f32 v138, v142, v48, v132
	v_fma_f32 v139, v142, v50, v133
	v_fmac_f32_e32 v140, v39, v18
	v_fmac_f32_e32 v141, v43, v18
	v_fmac_f32_e32 v138, v49, v18
	v_fmac_f32_e32 v139, v51, v18
	v_fmac_f32_e32 v140, v143, v40
	v_fmac_f32_e32 v141, v143, v44
	ds_write_b32 v163, v138 offset:5120
	v_fmac_f32_e32 v139, v143, v52
	v_fma_f32 v142, v41, v19, v140
	v_fmac_f32_e32 v141, v45, v19
	v_fmac_f32_e32 v139, v53, v19
	v_fmac_f32_e32 v141, v46, v142
	ds_write_b32 v163, v139 offset:5376
	v_fma_f32 v143, v47, v20, v141
	s_waitcnt lgkmcnt(2)
	ds_read_b128 v[2:5], v158 offset:3072
	ds_read_b128 v[6:9], v158 offset:3136
	ds_read_b128 v[10:13], v158 offset:3200
	ds_read_b128 v[14:17], v158 offset:3264
	ds_read_b128 v[30:33], v161 offset:34816
	ds_read_b128 v[34:37], v161 offset:34880
	ds_read_b128 v[18:21], v159 offset:16384
	ds_read_b128 v[22:25], v160 offset:26624
	ds_read_b128 v[26:29], v160 offset:26640
	ds_read_b128 v[38:41], v162 offset:37824
	ds_read_b128 v[42:45], v162 offset:37840
	ds_read_b128 v[46:49], v162 offset:37856
	ds_read_b128 v[50:53], v162 offset:37872
	v_cvt_pk_bf16_f32 v122, v54, v55
	v_cvt_pk_bf16_f32 v123, v56, v57
	v_cvt_pk_bf16_f32 v124, v58, v59
	v_cvt_pk_bf16_f32 v125, v60, v61
	v_cvt_pk_bf16_f32 v126, v62, v63
	v_cvt_pk_bf16_f32 v127, v64, v65
	v_cvt_pk_bf16_f32 v128, v66, v67
	v_cvt_pk_bf16_f32 v129, v68, v69
	v_mfma_f32_16x16x32_bf16 v[130:133], v[98:101], v[122:125], 0
	v_cvt_pk_bf16_f32 v136, v142, v86
	v_mfma_f32_16x16x32_bf16 v[130:133], v[102:105], v[126:129], v[130:133]
	v_cvt_pk_bf16_f32 v137, v143, v87
	v_cndmask_b32_e64 v134, 0, v136, s[40:41]
	v_cndmask_b32_e64 v135, 0, v137, s[40:41]
	v_mul_f32 v54, v54, v70
	v_mul_f32 v55, v55, v71
	v_mul_f32 v56, v56, v72
	v_mul_f32 v57, v57, v73
	v_mul_f32 v58, v58, v74
	v_mul_f32 v59, v59, v75
	v_mul_f32 v60, v60, v76
	v_mul_f32 v61, v61, v77
	v_mul_f32 v62, v62, v78
	v_mul_f32 v63, v63, v79
	v_mul_f32 v64, v64, v80
	v_mul_f32 v65, v65, v81
	v_mul_f32 v66, v66, v82
	v_mul_f32 v67, v67, v83
	v_mul_f32 v68, v68, v84
	v_mul_f32 v69, v69, v85
	v_mfma_f32_16x16x16_bf16 v[54:57], v[90:91], v[134:135], v[54:57]
	v_mfma_f32_16x16x16_bf16 v[58:61], v[92:93], v[134:135], v[58:61]
	v_mfma_f32_16x16x16_bf16 v[62:65], v[94:95], v[134:135], v[62:65]
	v_mfma_f32_16x16x16_bf16 v[66:69], v[96:97], v[134:135], v[66:69]
	v_fma_f32 v140, v142, v106, v130
	v_fma_f32 v141, v142, v110, v131
	v_fma_f32 v138, v142, v116, v132
	v_fma_f32 v139, v142, v118, v133
	v_fmac_f32_e32 v140, v107, v86
	v_fmac_f32_e32 v141, v111, v86
	v_fmac_f32_e32 v138, v117, v86
	v_fmac_f32_e32 v139, v119, v86
	v_fmac_f32_e32 v140, v143, v108
	v_fmac_f32_e32 v141, v143, v112
	ds_write_b32 v163, v138 offset:5632
	v_fmac_f32_e32 v139, v143, v120
	v_fma_f32 v142, v109, v87, v140
	v_fmac_f32_e32 v141, v113, v87
	v_fmac_f32_e32 v139, v121, v87
	v_fmac_f32_e32 v141, v114, v142
	ds_write_b32 v163, v139 offset:5888
	v_fma_f32 v143, v115, v88, v141
	s_waitcnt lgkmcnt(2)
; __device__ __forceinline__ void scan_load2(ScanOps& o, const LAS float* buf, const LAS float* vqp, const LAS unsigned char* bkp, int bkstep, int p, int lane) {
;     const int q = lane >> 4;
;     const LAS float* wp = buf + SC_WW + p * 64 + q * 4;
; #pragma unroll
;     for (int i = 0; i < 4; ++i) o.w[i] = *(const LAS f32x4*)(wp + 16 * i);
;     o.vq = *(const LAS f32x4*)(vqp + p * 256);
;     o.bk[0] = *(const LAS v4u*)(bkp + p * bkstep); o.bk[1] = *(const LAS v4u*)(bkp + p * bkstep + 16);
;     const LAS unsigned char* xp = (const LAS unsigned char*)(buf + SC_XA) + p * 512 + (lane & 3) * 128 + q * 16;
;     o.x[0] = *(const LAS bf16x8*)xp; o.x[1] = *(const LAS bf16x8*)(xp + 64);
; #pragma unroll
;     for (int i = 0; i < 4; ++i) o.c[i] = *(const LAS f32x4*)(buf + SC_C + p * 20 + 4 * i);
; }
; __device__ __forceinline__ const char* uni_ptr(const char* p) { const unsigned long long a = (unsigned long long)p;
;     const unsigned lo = (unsigned)__builtin_amdgcn_readfirstlane((int)(unsigned)a), hi = (unsigned)__builtin_amdgcn_readfirstlane((int)(unsigned)(a >> 32));
;     return (const char*)(((unsigned long long)hi << 32) | lo); }
; __device__ __forceinline__ float smul(float a, float b) { float r; asm("v_mul_f32 %0, %1, %2" : "=v"(r) : "v"(a), "v"(b)); return r; }
; __device__ __forceinline__ void scan_pair(const ScanOps& o, f32x4 (&St)[4], float& sa0, float& sa1, v4u (&am)[4], v4u& bm, LAS float* ypt, int ystep, unsigned m16) {
;     v4u s0, s1;
;     s0.x = cvt_pk_bf16(St[0].x, St[0].y); s0.y = cvt_pk_bf16(St[0].z, St[0].w); s0.z = cvt_pk_bf16(St[1].x, St[1].y); s0.w = cvt_pk_bf16(St[1].z, St[1].w);
;     s1.x = cvt_pk_bf16(St[2].x, St[2].y); s1.y = cvt_pk_bf16(St[2].z, St[2].w); s1.z = cvt_pk_bf16(St[3].x, St[3].y); s1.w = cvt_pk_bf16(St[3].z, St[3].w);
;     f32x4 dv = (f32x4){0.f, 0.f, 0.f, 0.f};
;     dv = __builtin_amdgcn_mfma_f32_16x16x32_bf16(o.x[0], __builtin_bit_cast(bf16x8, s0), dv, 0, 0, 0);
;     dv = __builtin_amdgcn_mfma_f32_16x16x32_bf16(o.x[1], __builtin_bit_cast(bf16x8, s1), dv, 0, 0, 0);
;     const float v0 = o.vq.x, v1 = o.vq.y, v2 = o.vq.z;
;     typedef short s16x4 __attribute__((ext_vector_type(4)));
;     const v2u bm2 = (v2u){cvt_pk_bf16(sa0, v0) & m16, cvt_pk_bf16(sa1, v1) & m16};
; #pragma unroll
;     for (int i = 0; i < 4; ++i) { const v2u a2 = (v2u){o.bk[i >> 1][(i & 1) * 2], o.bk[i >> 1][(i & 1) * 2 + 1]};
	ds_read_b128 v[70:73], v158 offset:3328
	ds_read_b128 v[74:77], v158 offset:3392
	ds_read_b128 v[78:81], v158 offset:3456
	ds_read_b128 v[82:85], v158 offset:3520
	ds_read_b128 v[98:101], v161 offset:35328
	ds_read_b128 v[102:105], v161 offset:35392
	ds_read_b128 v[86:89], v159 offset:17408
	ds_read_b128 v[90:93], v160 offset:27136
	ds_read_b128 v[94:97], v160 offset:27152
	ds_read_b128 v[106:109], v162 offset:37904
	ds_read_b128 v[110:113], v162 offset:37920
	ds_read_b128 v[114:117], v162 offset:37936
	ds_read_b128 v[118:121], v162 offset:37952
	v_cvt_pk_bf16_f32 v122, v54, v55
	v_cvt_pk_bf16_f32 v123, v56, v57
	v_cvt_pk_bf16_f32 v124, v58, v59
	v_cvt_pk_bf16_f32 v125, v60, v61
	v_cvt_pk_bf16_f32 v126, v62, v63
	v_cvt_pk_bf16_f32 v127, v64, v65
	v_cvt_pk_bf16_f32 v128, v66, v67
	v_cvt_pk_bf16_f32 v129, v68, v69
	v_mfma_f32_16x16x32_bf16 v[130:133], v[30:33], v[122:125], 0
	v_cvt_pk_bf16_f32 v136, v142, v18
	v_mfma_f32_16x16x32_bf16 v[130:133], v[34:37], v[126:129], v[130:133]
	v_cvt_pk_bf16_f32 v137, v143, v19
	v_cndmask_b32_e64 v134, 0, v136, s[40:41]
	v_cndmask_b32_e64 v135, 0, v137, s[40:41]
	v_mul_f32 v54, v54, v2
	v_mul_f32 v55, v55, v3
	v_mul_f32 v56, v56, v4
	v_mul_f32 v57, v57, v5
	v_mul_f32 v58, v58, v6
	v_mul_f32 v59, v59, v7
	v_mul_f32 v60, v60, v8
	v_mul_f32 v61, v61, v9
	v_mul_f32 v62, v62, v10
	v_mul_f32 v63, v63, v11
	v_mul_f32 v64, v64, v12
	v_mul_f32 v65, v65, v13
	v_mul_f32 v66, v66, v14
	v_mul_f32 v67, v67, v15
	v_mul_f32 v68, v68, v16
	v_mul_f32 v69, v69, v17
	v_mfma_f32_16x16x16_bf16 v[54:57], v[22:23], v[134:135], v[54:57]
	v_mfma_f32_16x16x16_bf16 v[58:61], v[24:25], v[134:135], v[58:61]
	v_mfma_f32_16x16x16_bf16 v[62:65], v[26:27], v[134:135], v[62:65]
	v_mfma_f32_16x16x16_bf16 v[66:69], v[28:29], v[134:135], v[66:69]
	v_fma_f32 v140, v142, v38, v130
	v_fma_f32 v141, v142, v42, v131
	v_fma_f32 v138, v142, v48, v132
	v_fma_f32 v139, v142, v50, v133
	v_fmac_f32_e32 v140, v39, v18
	v_fmac_f32_e32 v141, v43, v18
	v_fmac_f32_e32 v138, v49, v18
	v_fmac_f32_e32 v139, v51, v18
	v_fmac_f32_e32 v140, v143, v40
	v_fmac_f32_e32 v141, v143, v44
	ds_write_b32 v163, v138 offset:6144
	v_fmac_f32_e32 v139, v143, v52
	v_fma_f32 v142, v41, v19, v140
	v_fmac_f32_e32 v141, v45, v19
	v_fmac_f32_e32 v139, v53, v19
	v_fmac_f32_e32 v141, v46, v142
	ds_write_b32 v163, v139 offset:6400
	v_fma_f32 v143, v47, v20, v141
	s_waitcnt lgkmcnt(2)
	ds_read_b128 v[2:5], v158 offset:3584
	ds_read_b128 v[6:9], v158 offset:3648
	ds_read_b128 v[10:13], v158 offset:3712
	ds_read_b128 v[14:17], v158 offset:3776
	ds_read_b128 v[30:33], v161 offset:35840
	ds_read_b128 v[34:37], v161 offset:35904
	ds_read_b128 v[18:21], v159 offset:18432
	ds_read_b128 v[22:25], v160 offset:27648
	ds_read_b128 v[26:29], v160 offset:27664
	ds_read_b128 v[38:41], v162 offset:37984
	ds_read_b128 v[42:45], v162 offset:38000
	ds_read_b128 v[46:49], v162 offset:38016
	ds_read_b128 v[50:53], v162 offset:38032
	v_cvt_pk_bf16_f32 v122, v54, v55
	v_cvt_pk_bf16_f32 v123, v56, v57
	v_cvt_pk_bf16_f32 v124, v58, v59
	v_cvt_pk_bf16_f32 v125, v60, v61
	v_cvt_pk_bf16_f32 v126, v62, v63
	v_cvt_pk_bf16_f32 v127, v64, v65
	v_cvt_pk_bf16_f32 v128, v66, v67
	v_cvt_pk_bf16_f32 v129, v68, v69
	v_mfma_f32_16x16x32_bf16 v[130:133], v[98:101], v[122:125], 0
	v_cvt_pk_bf16_f32 v136, v142, v86
	v_mfma_f32_16x16x32_bf16 v[130:133], v[102:105], v[126:129], v[130:133]
	v_cvt_pk_bf16_f32 v137, v143, v87
	v_cndmask_b32_e64 v134, 0, v136, s[40:41]
	v_cndmask_b32_e64 v135, 0, v137, s[40:41]
	v_mul_f32 v54, v54, v70
	v_mul_f32 v55, v55, v71
	v_mul_f32 v56, v56, v72
	v_mul_f32 v57, v57, v73
	v_mul_f32 v58, v58, v74
	v_mul_f32 v59, v59, v75
	v_mul_f32 v60, v60, v76
	v_mul_f32 v61, v61, v77
	v_mul_f32 v62, v62, v78
	v_mul_f32 v63, v63, v79
	v_mul_f32 v64, v64, v80
	v_mul_f32 v65, v65, v81
	v_mul_f32 v66, v66, v82
	v_mul_f32 v67, v67, v83
	v_mul_f32 v68, v68, v84
	v_mul_f32 v69, v69, v85
	v_mfma_f32_16x16x16_bf16 v[54:57], v[90:91], v[134:135], v[54:57]
	v_mfma_f32_16x16x16_bf16 v[58:61], v[92:93], v[134:135], v[58:61]
	v_mfma_f32_16x16x16_bf16 v[62:65], v[94:95], v[134:135], v[62:65]
	v_mfma_f32_16x16x16_bf16 v[66:69], v[96:97], v[134:135], v[66:69]
	v_fma_f32 v140, v142, v106, v130
	v_fma_f32 v141, v142, v110, v131
	v_fma_f32 v138, v142, v116, v132
	v_fma_f32 v139, v142, v118, v133
	v_fmac_f32_e32 v140, v107, v86
	v_fmac_f32_e32 v141, v111, v86
	v_fmac_f32_e32 v138, v117, v86
	v_fmac_f32_e32 v139, v119, v86
	v_fmac_f32_e32 v140, v143, v108
	v_fmac_f32_e32 v141, v143, v112
	ds_write_b32 v163, v138 offset:6656
	v_fmac_f32_e32 v139, v143, v120
	v_fma_f32 v142, v109, v87, v140
	v_fmac_f32_e32 v141, v113, v87
	v_fmac_f32_e32 v139, v121, v87
	v_fmac_f32_e32 v141, v114, v142
	ds_write_b32 v163, v139 offset:6912
	v_fma_f32 v143, v115, v88, v141
	s_waitcnt lgkmcnt(2)
; __device__ __forceinline__ void scan_load2(ScanOps& o, const LAS float* buf, const LAS float* vqp, const LAS unsigned char* bkp, int bkstep, int p, int lane) {
;     const int q = lane >> 4;
;     const LAS float* wp = buf + SC_WW + p * 64 + q * 4;
; #pragma unroll
;     for (int i = 0; i < 4; ++i) o.w[i] = *(const LAS f32x4*)(wp + 16 * i);
;     o.vq = *(const LAS f32x4*)(vqp + p * 256);
;     o.bk[0] = *(const LAS v4u*)(bkp + p * bkstep); o.bk[1] = *(const LAS v4u*)(bkp + p * bkstep + 16);
;     const LAS unsigned char* xp = (const LAS unsigned char*)(buf + SC_XA) + p * 512 + (lane & 3) * 128 + q * 16;
;     o.x[0] = *(const LAS bf16x8*)xp; o.x[1] = *(const LAS bf16x8*)(xp + 64);
; #pragma unroll
;     for (int i = 0; i < 4; ++i) o.c[i] = *(const LAS f32x4*)(buf + SC_C + p * 20 + 4 * i);
; }
; __device__ __forceinline__ const char* uni_ptr(const char* p) { const unsigned long long a = (unsigned long long)p;
;     const unsigned lo = (unsigned)__builtin_amdgcn_readfirstlane((int)(unsigned)a), hi = (unsigned)__builtin_amdgcn_readfirstlane((int)(unsigned)(a >> 32));
;     return (const char*)(((unsigned long long)hi << 32) | lo); }
; __device__ __forceinline__ float smul(float a, float b) { float r; asm("v_mul_f32 %0, %1, %2" : "=v"(r) : "v"(a), "v"(b)); return r; }
; __device__ __forceinline__ void scan_pair(const ScanOps& o, f32x4 (&St)[4], float& sa0, float& sa1, v4u (&am)[4], v4u& bm, LAS float* ypt, int ystep, unsigned m16) {
;     v4u s0, s1;
;     s0.x = cvt_pk_bf16(St[0].x, St[0].y); s0.y = cvt_pk_bf16(St[0].z, St[0].w); s0.z = cvt_pk_bf16(St[1].x, St[1].y); s0.w = cvt_pk_bf16(St[1].z, St[1].w);
;     s1.x = cvt_pk_bf16(St[2].x, St[2].y); s1.y = cvt_pk_bf16(St[2].z, St[2].w); s1.z = cvt_pk_bf16(St[3].x, St[3].y); s1.w = cvt_pk_bf16(St[3].z, St[3].w);
;     f32x4 dv = (f32x4){0.f, 0.f, 0.f, 0.f};
;     dv = __builtin_amdgcn_mfma_f32_16x16x32_bf16(o.x[0], __builtin_bit_cast(bf16x8, s0), dv, 0, 0, 0);
;     dv = __builtin_amdgcn_mfma_f32_16x16x32_bf16(o.x[1], __builtin_bit_cast(bf16x8, s1), dv, 0, 0, 0);
;     const float v0 = o.vq.x, v1 = o.vq.y, v2 = o.vq.z;
;     typedef short s16x4 __attribute__((ext_vector_type(4)));
;     const v2u bm2 = (v2u){cvt_pk_bf16(sa0, v0) & m16, cvt_pk_bf16(sa1, v1) & m16};
; #pragma unroll
;     for (int i = 0; i < 4; ++i) { const v2u a2 = (v2u){o.bk[i >> 1][(i & 1) * 2], o.bk[i >> 1][(i & 1) * 2 + 1]};
	ds_read_b128 v[70:73], v158 offset:3840
	ds_read_b128 v[74:77], v158 offset:3904
	ds_read_b128 v[78:81], v158 offset:3968
	ds_read_b128 v[82:85], v158 offset:4032
	ds_read_b128 v[98:101], v161 offset:36352
	ds_read_b128 v[102:105], v161 offset:36416
	ds_read_b128 v[86:89], v159 offset:19456
	ds_read_b128 v[90:93], v160 offset:28160
	ds_read_b128 v[94:97], v160 offset:28176
	ds_read_b128 v[106:109], v162 offset:38064
	ds_read_b128 v[110:113], v162 offset:38080
	ds_read_b128 v[114:117], v162 offset:38096
	ds_read_b128 v[118:121], v162 offset:38112
	v_cvt_pk_bf16_f32 v122, v54, v55
	v_cvt_pk_bf16_f32 v123, v56, v57
	v_cvt_pk_bf16_f32 v124, v58, v59
	v_cvt_pk_bf16_f32 v125, v60, v61
	v_cvt_pk_bf16_f32 v126, v62, v63
	v_cvt_pk_bf16_f32 v127, v64, v65
	v_cvt_pk_bf16_f32 v128, v66, v67
	v_cvt_pk_bf16_f32 v129, v68, v69
	v_mfma_f32_16x16x32_bf16 v[130:133], v[30:33], v[122:125], 0
	v_cvt_pk_bf16_f32 v136, v142, v18
	v_mfma_f32_16x16x32_bf16 v[130:133], v[34:37], v[126:129], v[130:133]
	v_cvt_pk_bf16_f32 v137, v143, v19
	v_cndmask_b32_e64 v134, 0, v136, s[40:41]
	v_cndmask_b32_e64 v135, 0, v137, s[40:41]
	v_mul_f32 v54, v54, v2
	v_mul_f32 v55, v55, v3
	v_mul_f32 v56, v56, v4
	v_mul_f32 v57, v57, v5
	v_mul_f32 v58, v58, v6
	v_mul_f32 v59, v59, v7
	v_mul_f32 v60, v60, v8
	v_mul_f32 v61, v61, v9
	v_mul_f32 v62, v62, v10
	v_mul_f32 v63, v63, v11
	v_mul_f32 v64, v64, v12
	v_mul_f32 v65, v65, v13
	v_mul_f32 v66, v66, v14
	v_mul_f32 v67, v67, v15
	v_mul_f32 v68, v68, v16
	v_mul_f32 v69, v69, v17
	v_mfma_f32_16x16x16_bf16 v[54:57], v[22:23], v[134:135], v[54:57]
	v_mfma_f32_16x16x16_bf16 v[58:61], v[24:25], v[134:135], v[58:61]
	v_mfma_f32_16x16x16_bf16 v[62:65], v[26:27], v[134:135], v[62:65]
	v_mfma_f32_16x16x16_bf16 v[66:69], v[28:29], v[134:135], v[66:69]
	v_fma_f32 v140, v142, v38, v130
	v_fma_f32 v141, v142, v42, v131
	v_fma_f32 v138, v142, v48, v132
	v_fma_f32 v139, v142, v50, v133
	v_fmac_f32_e32 v140, v39, v18
	v_fmac_f32_e32 v141, v43, v18
	v_fmac_f32_e32 v138, v49, v18
	v_fmac_f32_e32 v139, v51, v18
	v_fmac_f32_e32 v140, v143, v40
	v_fmac_f32_e32 v141, v143, v44
	ds_write_b32 v163, v138 offset:7168
	v_fmac_f32_e32 v139, v143, v52
	v_fma_f32 v142, v41, v19, v140
	v_fmac_f32_e32 v141, v45, v19
	v_fmac_f32_e32 v139, v53, v19
	v_fmac_f32_e32 v141, v46, v142
	ds_write_b32 v163, v139 offset:7424
	v_fma_f32 v143, v47, v20, v141
	s_waitcnt lgkmcnt(2)
	v_cvt_pk_bf16_f32 v122, v54, v55
	v_cvt_pk_bf16_f32 v123, v56, v57
	v_cvt_pk_bf16_f32 v124, v58, v59
	v_cvt_pk_bf16_f32 v125, v60, v61
	v_cvt_pk_bf16_f32 v126, v62, v63
	v_cvt_pk_bf16_f32 v127, v64, v65
	v_cvt_pk_bf16_f32 v128, v66, v67
	v_cvt_pk_bf16_f32 v129, v68, v69
	v_mfma_f32_16x16x32_bf16 v[130:133], v[98:101], v[122:125], 0
	v_cvt_pk_bf16_f32 v136, v142, v86
	v_mfma_f32_16x16x32_bf16 v[130:133], v[102:105], v[126:129], v[130:133]
	v_cvt_pk_bf16_f32 v137, v143, v87
	v_cndmask_b32_e64 v134, 0, v136, s[40:41]
	v_cndmask_b32_e64 v135, 0, v137, s[40:41]
	v_mul_f32 v54, v54, v70
	v_mul_f32 v55, v55, v71
	v_mul_f32 v56, v56, v72
	v_mul_f32 v57, v57, v73
	v_mul_f32 v58, v58, v74
	v_mul_f32 v59, v59, v75
	v_mul_f32 v60, v60, v76
	v_mul_f32 v61, v61, v77
	v_mul_f32 v62, v62, v78
	v_mul_f32 v63, v63, v79
	v_mul_f32 v64, v64, v80
	v_mul_f32 v65, v65, v81
	v_mul_f32 v66, v66, v82
	v_mul_f32 v67, v67, v83
	v_mul_f32 v68, v68, v84
	v_mul_f32 v69, v69, v85
	v_mfma_f32_16x16x16_bf16 v[54:57], v[90:91], v[134:135], v[54:57]
	v_mfma_f32_16x16x16_bf16 v[58:61], v[92:93], v[134:135], v[58:61]
	v_mfma_f32_16x16x16_bf16 v[62:65], v[94:95], v[134:135], v[62:65]
	v_mfma_f32_16x16x16_bf16 v[66:69], v[96:97], v[134:135], v[66:69]
	v_fma_f32 v140, v142, v106, v130
	v_fma_f32 v141, v142, v110, v131
	v_fma_f32 v138, v142, v116, v132
	v_fma_f32 v139, v142, v118, v133
	v_fmac_f32_e32 v140, v107, v86
	v_fmac_f32_e32 v141, v111, v86
	v_fmac_f32_e32 v138, v117, v86
	v_fmac_f32_e32 v139, v119, v86
	v_fmac_f32_e32 v140, v143, v108
	v_fmac_f32_e32 v141, v143, v112
	ds_write_b32 v163, v138 offset:7680
	v_fmac_f32_e32 v139, v143, v120
	v_fma_f32 v142, v109, v87, v140
	v_fmac_f32_e32 v141, v113, v87
	v_fmac_f32_e32 v139, v121, v87
	v_fmac_f32_e32 v141, v114, v142
	ds_write_b32 v163, v139 offset:7936
	v_fma_f32 v143, v115, v88, v141
	s_branch .LBB0_1340
